# defer2 + P2 spatial-unit load ladders de-serialised (8 W loads issued at loop head, LN-stat batches merged) + split 7sp+6kv vs 1sp+2kv+tile
# baseline (speedup 1.0000x reference)
; #define LAS __attribute__((address_space(3)))
; __device__ __forceinline__ unsigned cvt_pk_bf16(float lo, float hi) { f32x2 v = {lo, hi}; bf16x2_t b = __builtin_convertvector(v, bf16x2_t); return __builtin_bit_cast(unsigned, b); }
; __device__ __forceinline__ void spatial_unit(Frame& F, const Args& a, int n, int g) {
;     ...
;     if (tid < 128) { const f32x4* p = (const f32x4*)(vstat + (size_t)(t0 + tid) * 32); float s = 0.f, q = 0.f;
; #pragma unroll
;         for (int j = 0; j < 8; ++j) { const f32x4 v = p[j]; s += v[0] + v[2]; q += v[1] + v[3]; }
;         const float mean = s * (1.f / GW), var = q * (1.f / GW) - mean * mean;
;         stats[2 * tid] = mean; stats[2 * tid + 1] = 1.0f / sqrtf(fmaxf(var, 0.f) + EPS); }
;     const float* ws_g = a.in[5] + (size_t)g * 128 * 128;
; #pragma unroll
;     for (int i = 0; i < 4; ++i) { const int id = tid + 512 * i, t = id >> 4, ch = id & 15;
;         const f32x4 x0 = *(const f32x4*)(ws_g + t * 128 + 8 * ch), x1 = *(const f32x4*)(ws_g + t * 128 + 8 * ch + 4);
;         float v[8] = {x0[0], x0[1], x0[2], x0[3], x1[0], x1[1], x1[2], x1[3]};
; #pragma unroll
;         for (int j = 0; j < 8; ++j) v[j] = (8 * ch + j <= t) ? v[j] : 0.f;
;         u32x4 o; o.x = cvt_pk_bf16(v[0], v[1]); o.y = cvt_pk_bf16(v[2], v[3]); o.z = cvt_pk_bf16(v[4], v[5]); o.w = cvt_pk_bf16(v[6], v[7]);
;         *(LAS u32x4*)(Wimg + off_b(t, ch)) = o; }
.LBB0_340:
	s_and_b32 s93, s91, 0xffffff80
	s_and_b32 s98, s92, 7
	s_lshl_b32 s98, s98, 16
	s_mov_b32 s99, 0
	v_lshl_add_u64 v[180:181], v[46:47], 0, s[98:99]
	v_lshl_add_u64 v[182:183], v[36:37], 2, v[180:181]
	global_load_dwordx4 v[184:187], v[182:183], off offset:16
	global_load_dwordx4 v[188:191], v[182:183], off
	v_lshl_add_u64 v[182:183], v[38:39], 2, v[180:181]
	global_load_dwordx4 v[192:195], v[182:183], off offset:16
	global_load_dwordx4 v[196:199], v[182:183], off
	v_lshl_add_u64 v[182:183], v[40:41], 2, v[180:181]
	global_load_dwordx4 v[200:203], v[182:183], off offset:16
	global_load_dwordx4 v[204:207], v[182:183], off
	v_lshl_add_u64 v[182:183], v[42:43], 2, v[180:181]
	global_load_dwordx4 v[208:211], v[182:183], off offset:16
	global_load_dwordx4 v[212:215], v[182:183], off
	s_and_saveexec_b64 s[88:89], s[6:7]
	s_cbranch_execz .LBB0_342
	v_add_u32_e32 v4, s93, v67
	v_ashrrev_i32_e32 v5, 31, v4
	v_lshlrev_b64 v[4:5], 7, v[4:5]
	v_lshl_add_u64 v[20:21], s[80:81], 0, v[4:5]
	global_load_dwordx4 v[4:7], v[20:21], off offset:48
	global_load_dwordx4 v[8:11], v[20:21], off offset:32
	global_load_dwordx4 v[12:15], v[20:21], off offset:16
	global_load_dwordx4 v[16:19], v[20:21], off
	global_load_dwordx4 v[216:219], v[20:21], off offset:112
	global_load_dwordx4 v[220:223], v[20:21], off offset:96
	global_load_dwordx4 v[224:227], v[20:21], off offset:80
	global_load_dwordx4 v[228:231], v[20:21], off offset:64
	s_mov_b32 s0, 0x3a800000
	s_waitcnt vmcnt(7)
	v_add_f32_e32 v4, v4, v6
	s_waitcnt vmcnt(6)
	v_add_f32_e32 v8, v8, v10
	s_waitcnt vmcnt(5)
	v_add_f32_e32 v12, v12, v14
	s_waitcnt vmcnt(4)
	v_add_f32_e32 v3, v16, v18
	v_add_f32_e32 v3, 0, v3
	v_add_f32_e32 v16, v17, v19
	v_add_f32_e32 v16, 0, v16
	v_add_f32_e32 v3, v3, v12
	v_add_f32_e32 v12, v13, v15
	v_add_f32_e32 v12, v16, v12
	v_add_f32_e32 v3, v3, v8
	v_add_f32_e32 v8, v9, v11
	v_add_f32_e32 v8, v12, v8
	v_add_f32_e32 v3, v3, v4
	v_add_f32_e32 v4, v5, v7
	v_add_f32_e32 v22, v8, v4
	s_waitcnt vmcnt(3)
	v_add_f32_e32 v216, v216, v218
	s_waitcnt vmcnt(2)
	v_add_f32_e32 v220, v220, v222
	s_waitcnt vmcnt(1)
	v_add_f32_e32 v224, v224, v226
	s_waitcnt vmcnt(0)
	v_add_f32_e32 v228, v228, v230
	v_add_f32_e32 v3, v3, v228
	v_add_f32_e32 v228, v229, v231
	v_add_f32_e32 v228, v22, v228
	v_add_f32_e32 v3, v3, v224
	v_add_f32_e32 v224, v225, v227
	v_add_f32_e32 v224, v228, v224
	v_add_f32_e32 v3, v3, v220
	v_add_f32_e32 v220, v221, v223
	v_add_f32_e32 v220, v224, v220
	v_add_f32_e32 v3, v3, v216
	v_add_f32_e32 v216, v217, v219
	v_add_f32_e32 v5, v220, v216
	v_mul_f32_e32 v4, 0x3a800000, v3
	v_mul_f32_e32 v3, v4, v4
	v_fma_f32 v3, v5, s0, -v3
	v_max_f32_e32 v3, 0, v3
	v_add_u32_e32 v5, 0, v77
	v_add_f32_e32 v3, 0x358637bd, v3
	s_mov_b32 s0, 0xf800000
	v_add_u32_e32 v6, 0x10000, v5
	v_cmp_gt_f32_e32 vcc, s0, v3
	v_mul_f32_e32 v5, 0x4f800000, v3
	s_nop 0
	v_cndmask_b32_e32 v3, v3, v5, vcc
	v_sqrt_f32_e32 v5, v3
	s_nop 0
	v_add_u32_e32 v7, -1, v5
	v_fma_f32 v8, -v7, v5, v3
	v_cmp_ge_f32_e64 s[0:1], 0, v8
	v_add_u32_e32 v8, 1, v5
	s_nop 0
	v_cndmask_b32_e64 v7, v5, v7, s[0:1]
	v_fma_f32 v5, -v8, v5, v3
	v_cmp_lt_f32_e64 s[0:1], 0, v5
	s_nop 1
	v_cndmask_b32_e64 v5, v7, v8, s[0:1]
	v_mul_f32_e32 v7, 0x37800000, v5
	v_cndmask_b32_e32 v5, v5, v7, vcc
	v_cmp_class_f32_e32 vcc, v3, v106
	s_nop 1
	v_cndmask_b32_e32 v3, v5, v3, vcc
	v_div_scale_f32 v5, s[0:1], v3, v3, 1.0
	v_rcp_f32_e32 v7, v5
	s_nop 0
	v_fma_f32 v8, -v5, v7, 1.0
	v_fmac_f32_e32 v7, v8, v7
	v_div_scale_f32 v8, vcc, 1.0, v3, 1.0
	v_mul_f32_e32 v9, v8, v7
	v_fma_f32 v10, -v5, v9, v8
	v_fmac_f32_e32 v9, v10, v7
	v_fma_f32 v5, -v5, v9, v8
	v_div_fmas_f32 v5, v5, v7, v9
	v_div_fixup_f32 v5, v5, v3, 1.0
	ds_write_b64 v6, v[4:5]
.LBB0_342:
	s_or_b64 exec, exec, s[88:89]
	s_and_b32 s0, s92, 7
	s_lshl_b32 s76, s0, 16
	s_lshl_b32 s76, s0, 8
	s_mov_b64 s[88:89], 0x10000
	s_add_i32 s1, 0, 0x10000
	s_andn2_b64 vcc, exec, s[74:75]
	v_add_u32_e32 v124, 0, v97
	v_add_u32_e32 v125, 0, v98
	v_add_u32_e32 v126, 0, v99
	v_add_u32_e32 v127, 0, v100
	v_add_u32_e32 v128, 0, v101
	v_add_u32_e32 v129, 0, v102
	v_add_u32_e32 v130, 0, v103
	v_add_u32_e32 v131, 0, v104
	s_waitcnt vmcnt(6)
	v_cndmask_b32_e64 v14, v185, 0, s[18:19]
	v_cndmask_b32_e64 v3, v188, 0, s[8:9]
	v_cndmask_b32_e64 v8, 0, v189, s[10:11]
	v_cndmask_b32_e64 v9, v190, 0, s[12:13]
	v_cndmask_b32_e64 v10, v191, 0, s[14:15]
	v_cndmask_b32_e64 v11, v184, 0, s[16:17]
	v_cndmask_b32_e64 v15, v186, 0, s[20:21]
	v_cndmask_b32_e64 v7, v187, 0, s[22:23]
	v_cvt_pk_bf16_f32 v4, v3, v8
	v_cvt_pk_bf16_f32 v5, v9, v10
	v_cvt_pk_bf16_f32 v6, v11, v14
	v_cvt_pk_bf16_f32 v7, v15, v7
	ds_write_b128 v66, v[4:7]
	s_waitcnt vmcnt(4)
	v_cndmask_b32_e64 v14, v193, 0, s[36:37]
	v_cndmask_b32_e64 v3, v196, 0, s[24:25]
	v_cndmask_b32_e64 v8, 0, v197, s[26:27]
	v_cndmask_b32_e64 v9, v198, 0, s[28:29]
	v_cndmask_b32_e64 v10, v199, 0, s[30:31]
	v_cndmask_b32_e64 v11, v192, 0, s[34:35]
	v_cndmask_b32_e64 v15, v194, 0, s[38:39]
	v_cndmask_b32_e64 v7, v195, 0, s[40:41]
	v_cvt_pk_bf16_f32 v4, v3, v8
	v_cvt_pk_bf16_f32 v5, v9, v10
	v_cvt_pk_bf16_f32 v6, v11, v14
	v_cvt_pk_bf16_f32 v7, v15, v7
	ds_write_b128 v107, v[4:7]
	s_waitcnt vmcnt(2)
	v_cndmask_b32_e64 v14, v201, 0, s[52:53]
	v_cndmask_b32_e64 v3, v204, 0, s[42:43]
	v_cndmask_b32_e64 v8, 0, v205, s[44:45]
	v_cndmask_b32_e64 v9, v206, 0, s[46:47]
	v_cndmask_b32_e64 v10, v207, 0, s[48:49]
	v_cndmask_b32_e64 v11, v200, 0, s[50:51]
	v_cndmask_b32_e64 v15, v202, 0, s[54:55]
	v_cndmask_b32_e64 v7, v203, 0, s[56:57]
	v_cvt_pk_bf16_f32 v4, v3, v8
	v_cvt_pk_bf16_f32 v5, v9, v10
	v_cvt_pk_bf16_f32 v6, v11, v14
	v_cvt_pk_bf16_f32 v7, v15, v7
	ds_write_b128 v108, v[4:7]
	s_waitcnt vmcnt(0)
	v_cndmask_b32_e64 v12, v209, 0, s[68:69]
	v_cndmask_b32_e64 v3, v212, 0, s[58:59]
	v_cndmask_b32_e64 v8, 0, v213, s[60:61]
	v_cndmask_b32_e64 v9, v214, 0, s[62:63]
	v_cndmask_b32_e64 v10, v215, 0, s[64:65]
	v_cndmask_b32_e64 v11, v208, 0, s[66:67]
	v_cndmask_b32_e64 v13, v210, 0, s[70:71]
	v_cndmask_b32_e64 v7, v211, 0, s[72:73]
	v_cvt_pk_bf16_f32 v4, v3, v8
	v_cvt_pk_bf16_f32 v5, v9, v10
	v_cvt_pk_bf16_f32 v6, v11, v12
	v_cvt_pk_bf16_f32 v7, v13, v7
	ds_write_b128 v109, v[4:7]
	v_add_u32_e32 v6, s93, v1
	v_ashrrev_i32_e32 v7, 31, v6
	v_lshl_add_u64 v[4:5], v[48:49], 0, s[76:77]
	v_lshlrev_b64 v[58:59], 11, v[6:7]
	v_lshl_add_u64 v[6:7], v[4:5], 0, v[58:59]
	v_lshl_add_u64 v[60:61], v[58:59], 0, s[88:89]
	s_mov_b64 s[88:89], 0x20000
	s_waitcnt lgkmcnt(0)
	s_barrier
; #define LAS __attribute__((address_space(3)))
; __device__ __forceinline__ unsigned cvt_pk_bf16(float lo, float hi) { f32x2 v = {lo, hi}; bf16x2_t b = __builtin_convertvector(v, bf16x2_t); return __builtin_bit_cast(unsigned, b); }
; __device__ __forceinline__ float bf_lo(unsigned w) { return __uint_as_float(w << 16); }
; __device__ __forceinline__ float bf_hi(unsigned w) { return __uint_as_float(w & 0xffff0000u); }
; __device__ __forceinline__ void spatial_unit(Frame& F, const Args& a, int n, int g) {
;     ...
;     const float* lng = a.in[3]; const float* lnb = a.in[4];
;     {
;         u32x4 xv[4]; const int ch = tid & 15;
; #pragma unroll
;         for (int i = 0; i < 4; ++i) xv[i] = __builtin_nontemporal_load((const u32x4*)(V + (size_t)(t0 + (tid >> 4) + 32 * i) * GW + ch0 + 8 * ch));
;         const f32x4 g0 = *(const f32x4*)(lng + ch0 + 8 * ch), g1 = *(const f32x4*)(lng + ch0 + 8 * ch + 4), b0 = *(const f32x4*)(lnb + ch0 + 8 * ch), b1 = *(const f32x4*)(lnb + ch0 + 8 * ch + 4);
; #pragma unroll
;         for (int i = 0; i < 4; ++i) { const int s = (tid >> 4) + 32 * i; const u32x4 x = xv[i];
;             const float mean = stats[2 * s], rstd = stats[2 * s + 1];
;             float v[8] = {bf_lo(x.x), bf_hi(x.x), bf_lo(x.y), bf_hi(x.y), bf_lo(x.z), bf_hi(x.z), bf_lo(x.w), bf_hi(x.w)};
; #pragma unroll
;             for (int j = 0; j < 4; ++j) { v[j] = (v[j] - mean) * rstd * g0[j] + b0[j]; v[4 + j] = (v[4 + j] - mean) * rstd * g1[j] + b1[j]; }
;             u32x4 o; o.x = cvt_pk_bf16(v[0], v[1]); o.y = cvt_pk_bf16(v[2], v[3]); o.z = cvt_pk_bf16(v[4], v[5]); o.w = cvt_pk_bf16(v[6], v[7]);
;             *(LAS u32x4*)(Vimg + off_b(s, ch)) = o; }
;     }
;     __syncthreads();
	global_load_dwordx4 v[28:31], v[6:7], off nt
	v_lshl_add_u64 v[62:63], v[58:59], 0, s[88:89]
	s_mov_b64 s[88:89], 0x30000
	v_lshl_add_u64 v[6:7], v[4:5], 0, v[60:61]
	v_lshl_add_u64 v[64:65], v[58:59], 0, s[88:89]
	s_lshl_b32 s76, s0, 9
	global_load_dwordx4 v[32:35], v[6:7], off nt
	v_lshl_add_u64 v[6:7], v[4:5], 0, v[62:63]
	v_lshl_add_u64 v[4:5], v[4:5], 0, v[64:65]
	v_lshl_add_u64 v[8:9], v[50:51], 0, s[76:77]
	v_lshl_add_u64 v[20:21], v[52:53], 0, s[76:77]
	global_load_dwordx4 v[24:27], v[6:7], off nt
	global_load_dwordx4 v[12:15], v[4:5], off nt
	s_nop 0
	global_load_dwordx4 v[4:7], v[8:9], off offset:16
	global_load_dwordx4 v[16:19], v[8:9], off
	s_nop 0
	global_load_dwordx4 v[8:11], v[20:21], off offset:16
	s_nop 0
	global_load_dwordx4 v[20:23], v[20:21], off
	v_add_u32_e32 v3, s1, v85
	ds_read_b64 v[116:117], v3
	v_add_u32_e32 v3, s1, v86
	s_waitcnt vmcnt(7)
	v_lshlrev_b32_e32 v118, 16, v28
	v_and_b32_e32 v119, 0xffff0000, v28
	v_lshlrev_b32_e32 v28, 16, v29
	v_and_b32_e32 v29, 0xffff0000, v29
	s_waitcnt lgkmcnt(0)
	v_pk_add_f32 v[28:29], v[28:29], v[116:117] op_sel_hi:[1,0] neg_lo:[0,1] neg_hi:[0,1]
	v_lshlrev_b32_e32 v120, 16, v30
	v_pk_mul_f32 v[28:29], v[116:117], v[28:29] op_sel:[1,0]
	v_and_b32_e32 v121, 0xffff0000, v30
	v_pk_add_f32 v[118:119], v[118:119], v[116:117] op_sel_hi:[1,0] neg_lo:[0,1] neg_hi:[0,1]
	v_pk_add_f32 v[120:121], v[120:121], v[116:117] op_sel_hi:[1,0] neg_lo:[0,1] neg_hi:[0,1]
	v_pk_mul_f32 v[118:119], v[116:117], v[118:119] op_sel:[1,0]
	v_pk_mul_f32 v[120:121], v[116:117], v[120:121] op_sel:[1,0]
	s_waitcnt vmcnt(0)
	v_pk_fma_f32 v[122:123], v[18:19], v[28:29], v[22:23]
	v_lshlrev_b32_e32 v28, 16, v31
	v_and_b32_e32 v29, 0xffff0000, v31
	v_pk_add_f32 v[28:29], v[28:29], v[116:117] op_sel_hi:[1,0] neg_lo:[0,1] neg_hi:[0,1]
	v_pk_fma_f32 v[118:119], v[16:17], v[118:119], v[20:21]
	v_pk_mul_f32 v[28:29], v[116:117], v[28:29] op_sel:[1,0]
	v_pk_fma_f32 v[120:121], v[4:5], v[120:121], v[8:9]
	v_pk_fma_f32 v[116:117], v[6:7], v[28:29], v[10:11]
	v_cvt_pk_bf16_f32 v28, v118, v119
	v_cvt_pk_bf16_f32 v29, v122, v123
	v_cvt_pk_bf16_f32 v30, v120, v121
	v_cvt_pk_bf16_f32 v31, v116, v117
	ds_write_b128 v66, v[28:31] offset:32768
	ds_read_b64 v[28:29], v3
	v_lshlrev_b32_e32 v30, 16, v32
	v_and_b32_e32 v31, 0xffff0000, v32
	v_lshlrev_b32_e32 v116, 16, v34
	v_and_b32_e32 v117, 0xffff0000, v34
	v_lshlrev_b32_e32 v32, 16, v33
	v_and_b32_e32 v33, 0xffff0000, v33
	v_lshlrev_b32_e32 v34, 16, v35
	v_and_b32_e32 v35, 0xffff0000, v35
	s_waitcnt lgkmcnt(0)
	v_pk_add_f32 v[30:31], v[30:31], v[28:29] op_sel_hi:[1,0] neg_lo:[0,1] neg_hi:[0,1]
	v_pk_add_f32 v[116:117], v[116:117], v[28:29] op_sel_hi:[1,0] neg_lo:[0,1] neg_hi:[0,1]
	v_pk_add_f32 v[32:33], v[32:33], v[28:29] op_sel_hi:[1,0] neg_lo:[0,1] neg_hi:[0,1]
	v_pk_add_f32 v[34:35], v[34:35], v[28:29] op_sel_hi:[1,0] neg_lo:[0,1] neg_hi:[0,1]
	v_pk_mul_f32 v[30:31], v[28:29], v[30:31] op_sel:[1,0]
	v_pk_mul_f32 v[116:117], v[28:29], v[116:117] op_sel:[1,0]
	v_pk_mul_f32 v[32:33], v[28:29], v[32:33] op_sel:[1,0]
	v_pk_mul_f32 v[28:29], v[28:29], v[34:35] op_sel:[1,0]
	v_pk_fma_f32 v[30:31], v[16:17], v[30:31], v[20:21]
	v_pk_fma_f32 v[116:117], v[4:5], v[116:117], v[8:9]
	v_pk_fma_f32 v[32:33], v[18:19], v[32:33], v[22:23]
	v_pk_fma_f32 v[34:35], v[6:7], v[28:29], v[10:11]
	v_cvt_pk_bf16_f32 v28, v30, v31
	v_cvt_pk_bf16_f32 v29, v32, v33
	v_cvt_pk_bf16_f32 v30, v116, v117
	v_cvt_pk_bf16_f32 v31, v34, v35
	v_add_u32_e32 v3, v81, v70
	ds_write_b128 v3, v[28:31] offset:32768
	v_add_u32_e32 v3, s1, v87
	ds_read_b64 v[28:29], v3
	v_lshlrev_b32_e32 v30, 16, v24
	v_and_b32_e32 v31, 0xffff0000, v24
	v_lshlrev_b32_e32 v24, 16, v25
	v_and_b32_e32 v25, 0xffff0000, v25
	s_waitcnt lgkmcnt(0)
	v_pk_add_f32 v[24:25], v[24:25], v[28:29] op_sel_hi:[1,0] neg_lo:[0,1] neg_hi:[0,1]
	v_lshlrev_b32_e32 v32, 16, v26
	v_pk_mul_f32 v[24:25], v[28:29], v[24:25] op_sel:[1,0]
	v_and_b32_e32 v33, 0xffff0000, v26
	v_pk_fma_f32 v[34:35], v[18:19], v[24:25], v[22:23]
	v_lshlrev_b32_e32 v24, 16, v27
	v_and_b32_e32 v25, 0xffff0000, v27
	v_pk_add_f32 v[30:31], v[30:31], v[28:29] op_sel_hi:[1,0] neg_lo:[0,1] neg_hi:[0,1]
	v_pk_add_f32 v[32:33], v[32:33], v[28:29] op_sel_hi:[1,0] neg_lo:[0,1] neg_hi:[0,1]
	v_pk_add_f32 v[24:25], v[24:25], v[28:29] op_sel_hi:[1,0] neg_lo:[0,1] neg_hi:[0,1]
	v_pk_mul_f32 v[30:31], v[28:29], v[30:31] op_sel:[1,0]
	v_pk_mul_f32 v[32:33], v[28:29], v[32:33] op_sel:[1,0]
	v_pk_mul_f32 v[24:25], v[28:29], v[24:25] op_sel:[1,0]
	v_pk_fma_f32 v[30:31], v[16:17], v[30:31], v[20:21]
	v_pk_fma_f32 v[32:33], v[4:5], v[32:33], v[8:9]
	v_pk_fma_f32 v[28:29], v[6:7], v[24:25], v[10:11]
	v_cvt_pk_bf16_f32 v24, v30, v31
	v_cvt_pk_bf16_f32 v25, v34, v35
	v_cvt_pk_bf16_f32 v26, v32, v33
	v_cvt_pk_bf16_f32 v27, v28, v29
	v_add_u32_e32 v3, v81, v71
	ds_write_b128 v3, v[24:27] offset:32768
	v_add_u32_e32 v3, s1, v88
	ds_read_b64 v[24:25], v3
	v_lshlrev_b32_e32 v26, 16, v12
	v_and_b32_e32 v27, 0xffff0000, v12
	v_add_u32_e32 v3, v81, v74
	v_add_u32_e32 v116, 0, v89
	s_waitcnt lgkmcnt(0)
	v_pk_add_f32 v[26:27], v[26:27], v[24:25] op_sel_hi:[1,0] neg_lo:[0,1] neg_hi:[0,1]
	v_add_u32_e32 v117, 0, v90
	v_pk_mul_f32 v[26:27], v[24:25], v[26:27] op_sel:[1,0]
	v_add_u32_e32 v118, 0, v91
	v_pk_fma_f32 v[16:17], v[16:17], v[26:27], v[20:21]
	v_lshlrev_b32_e32 v20, 16, v14
	v_and_b32_e32 v21, 0xffff0000, v14
	v_pk_add_f32 v[20:21], v[20:21], v[24:25] op_sel_hi:[1,0] neg_lo:[0,1] neg_hi:[0,1]
	v_add_u32_e32 v119, 0, v92
	v_pk_mul_f32 v[20:21], v[24:25], v[20:21] op_sel:[1,0]
	v_add_u32_e32 v120, 0, v93
	v_pk_fma_f32 v[8:9], v[4:5], v[20:21], v[8:9]
	v_lshlrev_b32_e32 v4, 16, v13
	v_and_b32_e32 v5, 0xffff0000, v13
	v_pk_add_f32 v[4:5], v[4:5], v[24:25] op_sel_hi:[1,0] neg_lo:[0,1] neg_hi:[0,1]
	v_add_u32_e32 v121, 0, v94
	v_pk_mul_f32 v[4:5], v[24:25], v[4:5] op_sel:[1,0]
	v_add_u32_e32 v122, 0, v95
	v_pk_fma_f32 v[12:13], v[18:19], v[4:5], v[22:23]
	v_lshlrev_b32_e32 v4, 16, v15
	v_and_b32_e32 v5, 0xffff0000, v15
	v_pk_add_f32 v[4:5], v[4:5], v[24:25] op_sel_hi:[1,0] neg_lo:[0,1] neg_hi:[0,1]
	v_add_u32_e32 v123, 0, v96
	v_pk_mul_f32 v[4:5], v[24:25], v[4:5] op_sel:[1,0]
	s_nop 0
	v_pk_fma_f32 v[10:11], v[6:7], v[4:5], v[10:11]
	v_cvt_pk_bf16_f32 v4, v16, v17
	v_cvt_pk_bf16_f32 v5, v12, v13
	v_cvt_pk_bf16_f32 v6, v8, v9
	v_cvt_pk_bf16_f32 v7, v10, v11
	ds_write_b128 v3, v[4:7] offset:32768
	s_waitcnt lgkmcnt(0)
	s_barrier
; #define LAS __attribute__((address_space(3)))
;     __device__ __forceinline__ const char* row_base(const pg8::Unit& u) const { return (const char*)((const int*)(ws + WS_ROWTOK) + (size_t)u.e * T + u.mt * 256 + u.hx * 128); }
; #define MFMA16(a, b, c) __builtin_amdgcn_mfma_f32_16x16x32_bf16(a, b, c, 0, 0, 0)
; __device__ __forceinline__ unsigned row_base(unsigned lane, unsigned s) { return row_addr16(lane, 0, s); }
; __device__ __forceinline__ unsigned tr_base(unsigned lane, unsigned c, unsigned t) { return tr_addr16(lane, c, 0, t); }
; __device__ __forceinline__ void spatial_unit(Frame& F, const Args& a, int n, int g) {
;     ...
;     const int ksmax = w >> 1;
;     {
;         unsigned vb[8][2];
; #pragma unroll
;         for (int c = 0; c < 8; ++c) { vb[c][0] = tr_base(lane, c, 0); vb[c][1] = tr_base(lane, c, 1); }
;         LAS unsigned char* Wrow = Wimg + 4096 * w;
; #pragma unroll
;         for (int ks = 0; ks < 4; ++ks) if (ks <= ksmax) {
;             const bf16x8 y = ROWF(Wrow, row_base(lane, ks), 0);
;             bf16x8 xf[8];
; #pragma unroll
;             for (int c = 0; c < 8; ++c) xf[c] = trf(Vimg, vb[c][0], vb[c][1], 8192 * ks);
;             __builtin_amdgcn_sched_barrier(0);
; #pragma unroll
;             for (int c = 0; c < 8; ++c) acc[c] = MFMA16(xf[c], y, acc[c]);
;             __builtin_amdgcn_sched_barrier(0);
;         }
	s_cbranch_vccnz .LBB0_344
	ds_read_b128 v[4:7], v110
	ds_read_b64_tr_b16 v[8:9], v116 offset:32768
	ds_read_b64_tr_b16 v[10:11], v117 offset:32768
	ds_read_b64_tr_b16 v[12:13], v118 offset:32768
	ds_read_b64_tr_b16 v[14:15], v119 offset:32768
	ds_read_b64_tr_b16 v[16:17], v120 offset:32768
	ds_read_b64_tr_b16 v[18:19], v121 offset:32768
	ds_read_b64_tr_b16 v[20:21], v122 offset:32768
	ds_read_b64_tr_b16 v[22:23], v123 offset:32768
	ds_read_b64_tr_b16 v[132:133], v124 offset:32768
	ds_read_b64_tr_b16 v[134:135], v125 offset:32768
	ds_read_b64_tr_b16 v[136:137], v126 offset:32768
	ds_read_b64_tr_b16 v[138:139], v127 offset:32768
	ds_read_b64_tr_b16 v[140:141], v128 offset:32768
	ds_read_b64_tr_b16 v[142:143], v129 offset:32768
	ds_read_b64_tr_b16 v[144:145], v130 offset:32768
	ds_read_b64_tr_b16 v[146:147], v131 offset:32768
	s_waitcnt lgkmcnt(14)
	v_mfma_f32_16x16x32_bf16 v[32:35], v[8:11], v[4:7], 0
	s_waitcnt lgkmcnt(12)
	v_mfma_f32_16x16x32_bf16 v[28:31], v[12:15], v[4:7], 0
	s_waitcnt lgkmcnt(10)
	v_mfma_f32_16x16x32_bf16 v[24:27], v[16:19], v[4:7], 0
	s_waitcnt lgkmcnt(8)
	v_mfma_f32_16x16x32_bf16 v[20:23], v[20:23], v[4:7], 0
	s_waitcnt lgkmcnt(6)
	v_mfma_f32_16x16x32_bf16 v[16:19], v[132:135], v[4:7], 0
	s_waitcnt lgkmcnt(4)
	v_mfma_f32_16x16x32_bf16 v[12:15], v[136:139], v[4:7], 0
	s_waitcnt lgkmcnt(2)
	v_mfma_f32_16x16x32_bf16 v[8:11], v[140:143], v[4:7], 0
	s_waitcnt lgkmcnt(0)
	v_mfma_f32_16x16x32_bf16 v[4:7], v[144:147], v[4:7], 0
	s_andn2_b64 vcc, exec, s[82:83]
	s_cbranch_vccz .LBB0_345
	s_branch .LBB0_346

; #define LAS __attribute__((address_space(3)))
; __device__ __forceinline__ float bf_lo(unsigned w) { return __uint_as_float(w << 16); }
; __device__ __forceinline__ void kv_unit(Frame& F, const Args& a, int c, int h) {
;     LAS unsigned char* Kimg = F.lds; LAS unsigned char* Vimg = F.lds + 32768;
;     const int t0 = c * 128, tid = F.tid, lane = F.lane, w = F.wave;
;     const bf16_t* Kb = (const bf16_t*)(F.ws + WS_K); const bf16_t* RV = (const bf16_t*)(F.ws + WS_RV); float* KV = (float*)(F.ws + WS_KV);
;     const float l2g = a.l2g[h];
;     {
;         u32x4 kx[4], vx[8];
; #pragma unroll
;         for (int i = 0; i < 4; ++i) kx[i] = __builtin_nontemporal_load((const u32x4*)(Kb + (size_t)(t0 + (tid >> 4) + 32 * i) * QKW + h * 128 + 8 * (tid & 15)));
; #pragma unroll
;         for (int i = 0; i < 8; ++i) vx[i] = __builtin_nontemporal_load((const u32x4*)(RV + (size_t)(t0 + (tid >> 5) + 16 * i) * D + h * 256 + 8 * (tid & 31)));
; #pragma unroll
;         for (int i = 0; i < 4; ++i) *(LAS u32x4*)(Kimg + off_b((tid >> 4) + 32 * i, tid & 15)) = kx[i];
; #pragma unroll
;         for (int i = 0; i < 8; ++i) { const int s = (tid >> 5) + 16 * i, ch = tid & 31; const u32x4 x = vx[i]; const float z = exp2f((float)(127 - s) * l2g);
;             u32x4 o; o.x = cvt_pk_bf16(bf_lo(x.x) * z, bf_hi(x.x) * z); o.y = cvt_pk_bf16(bf_lo(x.y) * z, bf_hi(x.y) * z); o.z = cvt_pk_bf16(bf_lo(x.z) * z, bf_hi(x.z) * z); o.w = cvt_pk_bf16(bf_lo(x.w) * z, bf_hi(x.w) * z);
;             *(LAS u32x4*)(Vimg + (ch >> 4) * 32768 + off_b(s, ch & 15)) = o; }
;     }
;     __syncthreads();
;     f32x4 acc[2][8];
; #pragma unroll
;     for (int j = 0; j < 2; ++j)
; #pragma unroll
;         for (int cd = 0; cd < 8; ++cd) acc[j][cd] = (f32x4){0.f, 0.f, 0.f, 0.f};
;     LAS unsigned char* vi = Vimg + (w >> 2) * 32768; const int cimg = (2 * w) & 7;
;     {
;         unsigned kb[8][2], vb[2][2];
; #pragma unroll
;         for (int cd = 0; cd < 8; ++cd) { kb[cd][0] = tr_base(lane, cd, 0); kb[cd][1] = tr_base(lane, cd, 1); }
; #pragma unroll
;         for (int j = 0; j < 2; ++j) { vb[j][0] = tr_base(lane, cimg + j, 0); vb[j][1] = tr_base(lane, cimg + j, 1); }
; __global__ void __launch_bounds__(NTHREADS, 2) mk_fwd(Args args) {
;     ...
;         for (int u = blockIdx.x; u < 1024; u += F.G) kv_unit(F, args, u >> 3, u & 7);
.LBB0_350:
	v_and_b32_e32 v2, 0x78, v77
	v_lshlrev_b32_e32 v2, 1, v2
	v_mov_b32_e32 v3, 0
	v_lshl_add_u64 v[4:5], s[94:95], 0, v[2:3]
	v_and_b32_e32 v2, 0xf8, v77
	s_mov_b64 s[0:1], 0x3e600000
	v_lshlrev_b32_e32 v2, 1, v2
	v_lshl_add_u64 v[10:11], v[4:5], 0, s[0:1]
	v_lshl_add_u64 v[4:5], s[94:95], 0, v[2:3]
	s_mov_b64 s[0:1], 0x40600000
	v_lshl_add_u64 v[12:13], v[4:5], 0, s[0:1]
	v_lshlrev_b32_e32 v4, 2, v83
	v_and_b32_e32 v4, 12, v4
	v_bitop3_b32 v4, v4, v68, v78 bitop3:0x36
	v_lshl_add_u32 v51, v4, 4, 0
	v_lshlrev_b32_e32 v4, 2, v82
	v_ashrrev_i32_e32 v32, 5, v67
	v_and_b32_e32 v4, 12, v4
	v_bitop3_b32 v4, v4, v68, v78 bitop3:0x36
	v_sub_u32_e32 v6, 0x7f, v32
	v_lshl_add_u32 v54, v4, 4, 0
	v_lshlrev_b32_e32 v4, 11, v67
	v_cvt_f32_i32_e32 v33, v6
	v_lshlrev_b32_e32 v6, 2, v32
	v_and_b32_e32 v4, 0x8000, v4
	v_bfe_u32 v5, v32, 2, 2
	v_and_b32_e32 v6, 12, v6
	v_add_u32_e32 v4, 0, v4
	v_bitop3_b32 v6, v6, v68, v5 bitop3:0x36
	v_lshl_add_u32 v56, v6, 4, v4
	v_add_u32_e32 v6, 16, v32
	v_lshlrev_b32_e32 v57, 8, v6
	v_lshlrev_b32_e32 v6, 2, v6
	v_and_b32_e32 v6, 12, v6
	v_bitop3_b32 v6, v6, v68, v5 bitop3:0x36
	v_lshl_add_u32 v58, v6, 4, v4
	v_add_u32_e32 v6, 32, v32
	v_lshlrev_b32_e32 v59, 8, v6
	v_lshlrev_b32_e32 v6, 2, v6
	v_and_b32_e32 v6, 12, v6
	v_bitop3_b32 v6, v6, v68, v5 bitop3:0x36
	v_lshl_add_u32 v60, v6, 4, v4
	v_add_u32_e32 v6, 48, v32
	v_lshlrev_b32_e32 v61, 8, v6
	v_lshlrev_b32_e32 v6, 2, v6
	v_and_b32_e32 v6, 12, v6
	v_bitop3_b32 v6, v6, v68, v5 bitop3:0x36
	v_lshl_add_u32 v62, v6, 4, v4
	v_add_u32_e32 v6, 64, v32
	v_lshlrev_b32_e32 v63, 8, v6
	v_lshlrev_b32_e32 v6, 2, v6
	v_and_b32_e32 v6, 12, v6
	v_bitop3_b32 v6, v6, v68, v5 bitop3:0x36
	v_lshl_add_u32 v64, v6, 4, v4
	v_add_u32_e32 v6, 0x50, v32
	v_lshlrev_b32_e32 v65, 8, v6
	v_lshlrev_b32_e32 v6, 2, v6
	v_and_b32_e32 v6, 12, v6
	v_lshlrev_b32_e32 v2, 2, v84
	v_bitop3_b32 v6, v6, v68, v5 bitop3:0x36
	v_and_b32_e32 v2, 12, v2
	v_lshl_add_u32 v77, v6, 4, v4
	v_add_u32_e32 v6, 0x60, v32
	v_bitop3_b32 v2, v2, v68, v78 bitop3:0x36
	v_lshlrev_b32_e32 v78, 8, v6
	v_lshlrev_b32_e32 v6, 2, v6
	v_sub_u32_e32 v7, 0x6f, v32
	v_and_b32_e32 v6, 12, v6
	v_cvt_f32_i32_e32 v34, v7
	v_sub_u32_e32 v7, 0x5f, v32
	v_bitop3_b32 v6, v6, v68, v5 bitop3:0x36
	v_cvt_f32_i32_e32 v35, v7
	v_sub_u32_e32 v7, 0x4f, v32
	v_lshl_add_u32 v81, v6, 4, v4
	v_add_u32_e32 v6, 0x70, v32
	v_cvt_f32_i32_e32 v46, v7
	v_sub_u32_e32 v7, 63, v32
	v_lshlrev_b32_e32 v82, 8, v6
	v_lshlrev_b32_e32 v6, 2, v6
	v_cvt_f32_i32_e32 v47, v7
	v_sub_u32_e32 v7, 47, v32
	v_and_b32_e32 v6, 12, v6
	s_lshl_b32 s6, s3, 2
	v_cvt_f32_i32_e32 v48, v7
	v_sub_u32_e32 v7, 31, v32
	v_bitop3_b32 v5, v6, v68, v5 bitop3:0x36
	s_lshl_b32 s0, s3, 13
	s_and_b32 s6, s6, 12
	v_cvt_f32_i32_e32 v49, v7
	v_sub_u32_e32 v7, 15, v32
	v_lshl_add_u32 v83, v5, 4, v4
	s_and_b32 s0, s0, 0xffff8000
	v_or_b32_e32 v4, s6, v45
	v_cvt_f32_i32_e32 v50, v7
	v_bitop3_b32 v7, v4, v79, 2 bitop3:0x36
	v_bitop3_b32 v4, v80, v4, 2 bitop3:0x1e
	s_add_i32 s0, s0, 0
	v_lshl_add_u32 v85, v4, 4, s0
	v_lshrrev_b32_e32 v4, 1, v67
	v_bitop3_b32 v5, s6, v79, v45 bitop3:0x36
	v_bitop3_b32 v6, v80, s6, v45 bitop3:0x1e
	v_and_b32_e32 v4, 24, v4
	v_readlane_b32 s92, v254, 12
	s_movk_i32 s99, 0x300
	s_cmpk_lt_i32 s92, 0x80
	s_cbranch_scc1 .Lp2_kv_go
	s_movk_i32 s99, 0x400
	s_addk_i32 s92, 0x280
